# sysnt
# speedup vs baseline: 1.0560x; 1.0307x over previous
_Z10gae_kernelPKfPKiS2_S0_S0_S0_PfS3_:
	s_load_dwordx8 s[4:11], s[0:1], 0x0
	s_load_dwordx4 s[12:15], s[0:1], 0x20
	v_and_b32_e32 v64, 63, v0
	v_lshrrev_b32_e32 v1, 6, v0
	s_mov_b32 s3, 0
	s_lshl_b64 s[2:3], s[2:3], 11
	v_lshlrev_b32_e32 v2, 9, v1
	v_lshlrev_b32_e32 v3, 2, v64
	v_or3_b32 v2, s2, v2, v3
	v_mov_b32_e32 v3, s3
	v_lshlrev_b64 v[18:19], 2, v[2:3]
	s_waitcnt lgkmcnt(0)
	v_lshl_add_u64 v[54:55], s[14:15], 0, v[18:19]
	v_lshl_add_u64 v[52:53], s[6:7], 0, v[18:19]
	global_load_dwordx4 v[10:13], v[54:55], off sc0 sc1 nt
	global_load_dwordx4 v[14:17], v[52:53], off sc0 sc1 nt
	v_lshl_add_u64 v[56:57], s[8:9], 0, v[18:19]
	global_load_dwordx4 v[20:23], v[56:57], off sc0 sc1 nt
	v_lshl_add_u64 v[58:59], s[12:13], 0, v[18:19]
	global_load_dwordx4 v[24:27], v[58:59], off sc0 sc1 nt
	v_lshl_add_u64 v[60:61], s[4:5], 0, v[18:19]
	global_load_dwordx4 v[28:31], v[60:61], off sc0 sc1 nt
	v_lshl_add_u64 v[62:63], s[10:11], 0, v[18:19]
	global_load_dwordx4 v[2:5], v[62:63], off sc0 sc1 nt
	global_load_dwordx4 v[32:35], v[60:61], off offset:1024 sc0 sc1 nt
	global_load_dwordx4 v[36:39], v[52:53], off offset:1024 sc0 sc1 nt
	global_load_dwordx4 v[40:43], v[56:57], off offset:1024 sc0 sc1 nt
	global_load_dwordx4 v[6:9], v[62:63], off offset:1024 sc0 sc1 nt
	global_load_dwordx4 v[44:47], v[58:59], off offset:1024 sc0 sc1 nt
	global_load_dwordx4 v[48:51], v[54:55], off offset:1024 sc0 sc1 nt
	v_mov_b32_e32 v66, 0
	v_mov_b32_e32 v68, 1.0
	v_mov_b32_e32 v69, 0
	v_mov_b32_e32 v70, 1.0
	v_mov_b32_e32 v71, 0
	v_mov_b32_e32 v72, 1.0
	v_bfe_u32 v73, v0, 4, 2
	v_cmp_gt_u32_e64 s[4:5], 16, v64
	v_mov_b32_e32 v65, 0
	v_mov_b32_e32 v67, 1.0
	s_waitcnt vmcnt(11)
	v_mul_f32_e32 v12, 0x3f7d70a4, v12
	s_waitcnt vmcnt(10)
	v_cmp_eq_u32_e32 vcc, 0, v14
	v_mul_f32_e32 v13, 0x3f7d70a4, v13
	v_mul_f32_e32 v10, 0x3f7d70a4, v10
	v_cndmask_b32_e64 v14, 0, 1.0, vcc
	s_waitcnt vmcnt(9)
	v_cmp_eq_u32_e32 vcc, 0, v20
	v_mul_f32_e32 v11, 0x3f7d70a4, v11
	s_waitcnt vmcnt(8)
	v_mul_f32_e32 v26, v26, v12
	v_cndmask_b32_e64 v20, 0, 1.0, vcc
	v_cmp_eq_u32_e32 vcc, 0, v15
	v_mul_f32_e32 v27, v27, v13
	v_mul_f32_e32 v24, v24, v10
	v_cndmask_b32_e64 v15, 0, 1.0, vcc
	v_cmp_eq_u32_e32 vcc, 0, v21
	v_mul_f32_e32 v25, v25, v11
	v_mul_f32_e32 v12, 0x3f733333, v12
	v_cndmask_b32_e64 v21, 0, 1.0, vcc
	v_cmp_eq_u32_e32 vcc, 0, v16
	v_mul_f32_e32 v13, 0x3f733333, v13
	v_mul_f32_e32 v10, 0x3f733333, v10
	v_cndmask_b32_e64 v16, 0, 1.0, vcc
	v_cmp_eq_u32_e32 vcc, 0, v22
	s_waitcnt vmcnt(7)
	v_fma_f32 v16, v26, v16, v30
	v_mul_f32_e32 v11, 0x3f733333, v11
	v_cndmask_b32_e64 v22, 0, 1.0, vcc
	v_cmp_eq_u32_e32 vcc, 0, v17
	v_fma_f32 v14, v24, v14, v28
	v_fma_f32 v15, v25, v15, v29
	v_cndmask_b32_e64 v17, 0, 1.0, vcc
	v_cmp_eq_u32_e32 vcc, 0, v23
	v_fmac_f32_e32 v31, v27, v17
	v_mul_f32_e32 v22, v12, v22
	v_cndmask_b32_e64 v23, 0, 1.0, vcc
	v_mul_f32_e32 v23, v13, v23
	s_waitcnt vmcnt(6)
	v_sub_f32_e32 v12, v16, v4
	v_sub_f32_e32 v13, v31, v5
	v_mul_f32_e32 v20, v10, v20
	v_mul_f32_e32 v21, v11, v21
	v_sub_f32_e32 v10, v14, v2
	v_sub_f32_e32 v11, v15, v3
	v_mul_f32_e32 v14, v23, v22
	v_fma_f32 v15, v22, v13, v12
	v_mul_f32_e32 v14, v14, v21
	v_fma_f32 v15, v21, v15, v11
	v_mul_f32_e32 v14, v14, v20
	v_fma_f32 v24, v20, v15, v10
	v_mov_b32_e32 v16, 1.0
	v_mov_b32_dpp v68, v14 row_shl:1 row_mask:0xf bank_mask:0xf
	v_mov_b32_dpp v66, v24 row_shl:1 row_mask:0xf bank_mask:0xf
	v_mul_f32_e32 v15, v14, v68
	v_fmac_f32_e32 v24, v14, v66
	v_cmp_eq_u32_e32 vcc, 2, v73
	v_mov_b32_dpp v70, v15 row_shl:2 row_mask:0xf bank_mask:0xf
	v_mov_b32_dpp v69, v24 row_shl:2 row_mask:0xf bank_mask:0xf
	v_mul_f32_e32 v14, v15, v70
	v_fmac_f32_e32 v24, v15, v69
	v_mov_b32_e32 v15, 0
	v_mov_b32_dpp v72, v14 row_shl:4 row_mask:0xf bank_mask:0xf
	v_mov_b32_dpp v71, v24 row_shl:4 row_mask:0xf bank_mask:0xf
	v_fmac_f32_e32 v24, v14, v71
	v_mul_f32_e32 v14, v14, v72
	s_nop 0
	v_mov_b32_dpp v15, v24 row_shl:8 row_mask:0xf bank_mask:0xf
	v_mov_b32_dpp v16, v14 row_shl:8 row_mask:0xf bank_mask:0xf
	v_fmac_f32_e32 v24, v14, v15
	v_mul_f32_e32 v14, v14, v16
	v_readlane_b32 s9, v24, 32
	v_readlane_b32 s2, v14, 48
	v_readlane_b32 s8, v14, 32
	v_readlane_b32 s6, v14, 16
	v_mov_b32_e32 v15, s2
	v_mul_f32_e32 v16, s8, v15
	v_cndmask_b32_e32 v15, 1.0, v15, vcc
	v_cmp_eq_u32_e64 s[2:3], 1, v73
	v_readlane_b32 s10, v24, 48
	v_mul_f32_e32 v17, s6, v16
	v_cndmask_b32_e64 v15, v15, v16, s[2:3]
	v_readlane_b32 s7, v24, 16
	v_cndmask_b32_e64 v15, v15, v17, s[4:5]
	v_mov_b32_e32 v16, s9
	v_mov_b32_e32 v17, s10
	v_fmac_f32_e32 v16, s8, v17
	v_mov_b32_e32 v25, s7
	v_cndmask_b32_e32 v17, 0, v17, vcc
	v_fmac_f32_e32 v25, s6, v16
	v_cndmask_b32_e64 v16, v17, v16, s[2:3]
	v_cndmask_b32_e64 v16, v16, v25, s[4:5]
	s_waitcnt vmcnt(4)
	v_cmp_eq_u32_e64 s[6:7], 0, v36
	v_fmac_f32_e32 v24, v14, v16
	v_mul_f32_e32 v28, v14, v15
	s_waitcnt vmcnt(0)
	v_mul_f32_e32 v15, 0x3f7d70a4, v48
	v_cndmask_b32_e64 v14, 0, 1.0, s[6:7]
	v_cmp_eq_u32_e64 s[6:7], 0, v40
	v_mul_f32_e32 v17, v44, v15
	v_mul_f32_e32 v15, 0x3f733333, v15
	v_cndmask_b32_e64 v16, 0, 1.0, s[6:7]
	v_cmp_eq_u32_e64 s[6:7], 0, v37
	v_mul_f32_e32 v25, v15, v16
	v_mul_f32_e32 v16, 0x3f7d70a4, v49
	v_cndmask_b32_e64 v15, 0, 1.0, s[6:7]
	v_cmp_eq_u32_e64 s[6:7], 0, v41
	v_fma_f32 v14, v17, v14, v32
	v_mul_f32_e32 v26, v45, v16
	v_cndmask_b32_e64 v17, 0, 1.0, s[6:7]
	v_mul_f32_e32 v16, 0x3f733333, v16
	v_fma_f32 v15, v26, v15, v33
	v_mul_f32_e32 v26, v16, v17
	v_mul_f32_e32 v17, 0x3f7d70a4, v50
	v_cmp_eq_u32_e64 s[6:7], 0, v38
	v_mul_f32_e32 v29, v46, v17
	v_mul_f32_e32 v17, 0x3f733333, v17
	v_cndmask_b32_e64 v16, 0, 1.0, s[6:7]
	v_cmp_eq_u32_e64 s[6:7], 0, v42
	v_fma_f32 v16, v29, v16, v34
	v_mul_f32_e32 v29, 0x3f7d70a4, v51
	v_cndmask_b32_e64 v27, 0, 1.0, s[6:7]
	v_cmp_eq_u32_e64 s[6:7], 0, v39
	v_mul_f32_e32 v27, v17, v27
	v_mul_f32_e32 v31, v47, v29
	v_cndmask_b32_e64 v17, 0, 1.0, s[6:7]
	v_cmp_eq_u32_e64 s[6:7], 0, v43
	v_fmac_f32_e32 v35, v31, v17
	v_mul_f32_e32 v29, 0x3f733333, v29
	v_cndmask_b32_e64 v30, 0, 1.0, s[6:7]
	v_sub_f32_e32 v16, v16, v8
	v_sub_f32_e32 v17, v35, v9
	v_mul_f32_e32 v29, v29, v30
	v_sub_f32_e32 v15, v15, v7
	v_fma_f32 v30, v27, v17, v16
	v_mul_f32_e32 v31, v29, v27
	v_sub_f32_e32 v14, v14, v6
	v_fma_f32 v30, v26, v30, v15
	v_mul_f32_e32 v31, v31, v26
	v_fma_f32 v30, v25, v30, v14
	v_mul_f32_e32 v31, v31, v25
	v_mov_b32_e32 v32, 0
	v_mov_b32_e32 v33, 1.0
	s_nop 0
	v_mov_b32_dpp v32, v30 row_shl:1 row_mask:0xf bank_mask:0xf
	v_mov_b32_dpp v33, v31 row_shl:1 row_mask:0xf bank_mask:0xf
	v_fmac_f32_e32 v30, v31, v32
	v_mul_f32_e32 v31, v31, v33
	v_mov_b32_e32 v32, 0
	v_mov_b32_e32 v33, 1.0
	s_nop 0
	v_mov_b32_dpp v32, v30 row_shl:2 row_mask:0xf bank_mask:0xf
	v_mov_b32_dpp v33, v31 row_shl:2 row_mask:0xf bank_mask:0xf
	v_fmac_f32_e32 v30, v31, v32
	v_mul_f32_e32 v31, v31, v33
	v_mov_b32_e32 v32, 0
	v_mov_b32_e32 v33, 1.0
	s_nop 0
	v_mov_b32_dpp v32, v30 row_shl:4 row_mask:0xf bank_mask:0xf
	v_mov_b32_dpp v33, v31 row_shl:4 row_mask:0xf bank_mask:0xf
	v_fmac_f32_e32 v30, v31, v32
	v_mul_f32_e32 v31, v31, v33
	s_nop 0
	v_mov_b32_dpp v65, v30 row_shl:8 row_mask:0xf bank_mask:0xf
	v_mov_b32_dpp v67, v31 row_shl:8 row_mask:0xf bank_mask:0xf
	v_fmac_f32_e32 v30, v31, v65
	v_mul_f32_e32 v31, v31, v67
	v_readlane_b32 s9, v30, 32
	v_readlane_b32 s10, v31, 48
	v_readlane_b32 s8, v31, 32
	v_readlane_b32 s6, v31, 16
	v_mov_b32_e32 v32, s10
	v_mul_f32_e32 v33, s8, v32
	v_cndmask_b32_e32 v32, 1.0, v32, vcc
	v_readlane_b32 s11, v30, 48
	v_mul_f32_e32 v34, s6, v33
	v_cndmask_b32_e64 v32, v32, v33, s[2:3]
	v_readlane_b32 s7, v30, 16
	v_cndmask_b32_e64 v32, v32, v34, s[4:5]
	v_mov_b32_e32 v33, s9
	v_mov_b32_e32 v34, s11
	v_fmac_f32_e32 v33, s8, v34
	v_mov_b32_e32 v35, s7
	v_cndmask_b32_e32 v34, 0, v34, vcc
	v_fmac_f32_e32 v35, s6, v33
	v_cndmask_b32_e64 v33, v34, v33, s[2:3]
	v_cndmask_b32_e64 v33, v33, v35, s[4:5]
	v_fmac_f32_e32 v30, v31, v33
	v_mul_f32_e32 v31, v31, v32
	v_readlane_b32 s6, v28, 0
	v_readlane_b32 s7, v24, 0
	v_readlane_b32 s4, v31, 0
	v_readlane_b32 s5, v30, 0
	v_cmp_eq_u32_e32 vcc, 0, v64
	s_and_saveexec_b64 s[2:3], vcc
	s_cbranch_execz .LBB0_4
	v_mov_b32_e32 v32, s4
	v_mov_b32_e32 v33, s7
	v_mov_b32_e32 v34, s5
	v_mul_f32_e32 v32, s6, v32
	v_lshlrev_b32_e32 v1, 2, v1
	v_fmac_f32_e32 v33, s6, v34
	ds_write2_b32 v1, v32, v33 offset1:4
